# router pass B: all sixteen 16-byte pieces of the lane's k-run requested at the top of the pass (free registers), copies behind counted waits where the original single-load waits stood
# speedup vs baseline: 1.0004x; 1.0004x over previous
.LBB0_654:
	v_add_u32_e32 v4, s33, v112
	v_or_b32_e32 v0, v4, v111
	v_ashrrev_i32_e32 v1, 31, v0
	v_lshlrev_b64 v[0:1], 11, v[0:1]
	v_lshl_add_u64 v[0:1], v[38:39], 0, v[0:1]
	global_load_dwordx4 v[152:155], v[0:1], off
	global_load_dwordx4 v[156:159], v[0:1], off offset:16
	global_load_dwordx4 v[160:163], v[0:1], off offset:32
	global_load_dwordx4 v[164:167], v[0:1], off offset:48
	global_load_dwordx4 v[168:171], v[0:1], off offset:64
	global_load_dwordx4 v[172:175], v[0:1], off offset:80
	global_load_dwordx4 v[176:179], v[0:1], off offset:96
	global_load_dwordx4 v[180:183], v[0:1], off offset:112
	global_load_dwordx4 v[188:191], v[0:1], off offset:128
	global_load_dwordx4 v[192:195], v[0:1], off offset:144
	global_load_dwordx4 v[196:199], v[0:1], off offset:160
	global_load_dwordx4 v[200:203], v[0:1], off offset:176
	global_load_dwordx4 v[204:207], v[0:1], off offset:192
	global_load_dwordx4 v[208:211], v[0:1], off offset:208
	global_load_dwordx4 v[212:215], v[0:1], off offset:224
	global_load_dwordx4 v[216:219], v[0:1], off offset:240
	ds_read_b128 v[14:17], v123
	ds_read_b128 v[18:21], v123 offset:256
	s_waitcnt vmcnt(15)
	v_mov_b64_e32 v[6:7], v[152:153]
	v_mov_b64_e32 v[8:9], v[154:155]
	v_cvt_f32_f16_e32 v2, v6
	s_waitcnt vmcnt(14)
	v_mov_b64_e32 v[10:11], v[156:157]
	v_mov_b64_e32 v[12:13], v[158:159]
	v_cvt_f32_f16_sdwa v3, v13 dst_sel:DWORD dst_unused:UNUSED_PAD src0_sel:WORD_1
	s_waitcnt lgkmcnt(1)
	v_mfma_f32_16x16x4_f32 v[22:25], v2, v14, 0
	v_cvt_f32_f16_sdwa v2, v6 dst_sel:DWORD dst_unused:UNUSED_PAD src0_sel:WORD_1
	s_nop 1
	v_mfma_f32_16x16x4_f32 v[22:25], v2, v15, v[22:25]
	v_cvt_f32_f16_e32 v2, v7
	s_nop 1
	v_mfma_f32_16x16x4_f32 v[22:25], v2, v16, v[22:25]
	v_cvt_f32_f16_sdwa v2, v7 dst_sel:DWORD dst_unused:UNUSED_PAD src0_sel:WORD_1
	s_nop 1
	v_mfma_f32_16x16x4_f32 v[14:17], v2, v17, v[22:25]
	v_cvt_f32_f16_e32 v2, v8
	s_nop 4
	s_nop 0
	s_waitcnt lgkmcnt(0)
	v_mfma_f32_16x16x4_f32 v[14:17], v2, v18, v[14:17]
	v_cvt_f32_f16_sdwa v2, v8 dst_sel:DWORD dst_unused:UNUSED_PAD src0_sel:WORD_1
	s_nop 1
	v_mfma_f32_16x16x4_f32 v[14:17], v2, v19, v[14:17]
	v_cvt_f32_f16_e32 v2, v9
	s_nop 1
	v_mfma_f32_16x16x4_f32 v[14:17], v2, v20, v[14:17]
	v_cvt_f32_f16_sdwa v2, v9 dst_sel:DWORD dst_unused:UNUSED_PAD src0_sel:WORD_1
	s_nop 1
	v_mfma_f32_16x16x4_f32 v[6:9], v2, v21, v[14:17]
	v_cvt_f32_f16_e32 v2, v10
	s_nop 4
	ds_read_b128 v[14:17], v123 offset:512
	ds_read_b128 v[18:21], v123 offset:768
	s_waitcnt lgkmcnt(1)
	v_mfma_f32_16x16x4_f32 v[6:9], v2, v14, v[6:9]
	v_cvt_f32_f16_sdwa v2, v10 dst_sel:DWORD dst_unused:UNUSED_PAD src0_sel:WORD_1
	s_nop 1
	v_mfma_f32_16x16x4_f32 v[6:9], v2, v15, v[6:9]
	v_cvt_f32_f16_e32 v2, v11
	s_nop 1
	v_mfma_f32_16x16x4_f32 v[6:9], v2, v16, v[6:9]
	v_cvt_f32_f16_sdwa v2, v11 dst_sel:DWORD dst_unused:UNUSED_PAD src0_sel:WORD_1
	s_nop 1
	v_mfma_f32_16x16x4_f32 v[6:9], v2, v17, v[6:9]
	v_cvt_f32_f16_e32 v2, v12
	s_waitcnt lgkmcnt(0)
	s_nop 0
	v_mfma_f32_16x16x4_f32 v[6:9], v2, v18, v[6:9]
	v_cvt_f32_f16_sdwa v2, v12 dst_sel:DWORD dst_unused:UNUSED_PAD src0_sel:WORD_1
	s_nop 1
	v_mfma_f32_16x16x4_f32 v[6:9], v2, v19, v[6:9]
	v_cvt_f32_f16_e32 v2, v13
	s_nop 0
	s_nop 0
	v_mfma_f32_16x16x4_f32 v[6:9], v2, v20, v[6:9]
	s_waitcnt vmcnt(13)
	v_mov_b64_e32 v[22:23], v[160:161]
	v_mov_b64_e32 v[24:25], v[162:163]
	v_cvt_f32_f16_e32 v2, v22
	v_mfma_f32_16x16x4_f32 v[6:9], v3, v21, v[6:9]
	ds_read_b128 v[14:17], v123 offset:1024
	ds_read_b128 v[18:21], v123 offset:1280
	s_waitcnt vmcnt(12)
	v_mov_b64_e32 v[10:11], v[164:165]
	v_mov_b64_e32 v[12:13], v[166:167]
	v_cvt_f32_f16_sdwa v3, v13 dst_sel:DWORD dst_unused:UNUSED_PAD src0_sel:WORD_1
	s_waitcnt lgkmcnt(1)
	v_mfma_f32_16x16x4_f32 v[6:9], v2, v14, v[6:9]
	v_cvt_f32_f16_sdwa v2, v22 dst_sel:DWORD dst_unused:UNUSED_PAD src0_sel:WORD_1
	s_nop 1
	v_mfma_f32_16x16x4_f32 v[6:9], v2, v15, v[6:9]
	v_cvt_f32_f16_e32 v2, v23
	s_nop 1
	v_mfma_f32_16x16x4_f32 v[6:9], v2, v16, v[6:9]
	v_cvt_f32_f16_sdwa v2, v23 dst_sel:DWORD dst_unused:UNUSED_PAD src0_sel:WORD_1
	s_nop 1
	v_mfma_f32_16x16x4_f32 v[6:9], v2, v17, v[6:9]
	v_cvt_f32_f16_e32 v2, v24
	s_nop 0
	s_waitcnt lgkmcnt(0)
	v_mfma_f32_16x16x4_f32 v[6:9], v2, v18, v[6:9]
	v_cvt_f32_f16_sdwa v2, v24 dst_sel:DWORD dst_unused:UNUSED_PAD src0_sel:WORD_1
	s_nop 1
	v_mfma_f32_16x16x4_f32 v[6:9], v2, v19, v[6:9]
	v_cvt_f32_f16_e32 v2, v25
	s_nop 1
	v_mfma_f32_16x16x4_f32 v[6:9], v2, v20, v[6:9]
	v_cvt_f32_f16_sdwa v2, v25 dst_sel:DWORD dst_unused:UNUSED_PAD src0_sel:WORD_1
	s_nop 1
	v_mfma_f32_16x16x4_f32 v[6:9], v2, v21, v[6:9]
	v_cvt_f32_f16_e32 v2, v10
	ds_read_b128 v[18:21], v123 offset:1536
	ds_read_b128 v[22:25], v123 offset:1792
	s_waitcnt lgkmcnt(1)
	v_mfma_f32_16x16x4_f32 v[6:9], v2, v18, v[6:9]
	v_cvt_f32_f16_sdwa v2, v10 dst_sel:DWORD dst_unused:UNUSED_PAD src0_sel:WORD_1
	s_nop 1
	v_mfma_f32_16x16x4_f32 v[6:9], v2, v19, v[6:9]
	v_cvt_f32_f16_e32 v2, v11
	s_nop 1
	v_mfma_f32_16x16x4_f32 v[6:9], v2, v20, v[6:9]
	v_cvt_f32_f16_sdwa v2, v11 dst_sel:DWORD dst_unused:UNUSED_PAD src0_sel:WORD_1
	s_nop 1
	v_mfma_f32_16x16x4_f32 v[6:9], v2, v21, v[6:9]
	v_cvt_f32_f16_e32 v2, v12
	s_waitcnt lgkmcnt(0)
	s_nop 0
	v_mfma_f32_16x16x4_f32 v[6:9], v2, v22, v[6:9]
	v_cvt_f32_f16_sdwa v2, v12 dst_sel:DWORD dst_unused:UNUSED_PAD src0_sel:WORD_1
	s_nop 1
	v_mfma_f32_16x16x4_f32 v[6:9], v2, v23, v[6:9]
	v_cvt_f32_f16_e32 v2, v13
	s_nop 0
	s_nop 0
	v_mfma_f32_16x16x4_f32 v[6:9], v2, v24, v[6:9]
	s_waitcnt vmcnt(11)
	v_mov_b64_e32 v[14:15], v[168:169]
	v_mov_b64_e32 v[16:17], v[170:171]
	v_cvt_f32_f16_e32 v2, v14
	v_mfma_f32_16x16x4_f32 v[6:9], v3, v25, v[6:9]
	ds_read_b128 v[18:21], v123 offset:2048
	ds_read_b128 v[22:25], v123 offset:2304
	s_waitcnt vmcnt(10)
	v_mov_b64_e32 v[10:11], v[172:173]
	v_mov_b64_e32 v[12:13], v[174:175]
	v_cvt_f32_f16_sdwa v3, v13 dst_sel:DWORD dst_unused:UNUSED_PAD src0_sel:WORD_1
	s_waitcnt lgkmcnt(1)
	v_mfma_f32_16x16x4_f32 v[6:9], v2, v18, v[6:9]
	v_cvt_f32_f16_sdwa v2, v14 dst_sel:DWORD dst_unused:UNUSED_PAD src0_sel:WORD_1
	s_nop 1
	v_mfma_f32_16x16x4_f32 v[6:9], v2, v19, v[6:9]
	v_cvt_f32_f16_e32 v2, v15
	s_nop 1
	v_mfma_f32_16x16x4_f32 v[6:9], v2, v20, v[6:9]
	v_cvt_f32_f16_sdwa v2, v15 dst_sel:DWORD dst_unused:UNUSED_PAD src0_sel:WORD_1
	s_nop 1
	v_mfma_f32_16x16x4_f32 v[6:9], v2, v21, v[6:9]
	v_cvt_f32_f16_e32 v2, v16
	s_nop 0
	s_waitcnt lgkmcnt(0)
	v_mfma_f32_16x16x4_f32 v[6:9], v2, v22, v[6:9]
	v_cvt_f32_f16_sdwa v2, v16 dst_sel:DWORD dst_unused:UNUSED_PAD src0_sel:WORD_1
	s_nop 1
	v_mfma_f32_16x16x4_f32 v[6:9], v2, v23, v[6:9]
	v_cvt_f32_f16_e32 v2, v17
	s_nop 1
	v_mfma_f32_16x16x4_f32 v[6:9], v2, v24, v[6:9]
	v_cvt_f32_f16_sdwa v2, v17 dst_sel:DWORD dst_unused:UNUSED_PAD src0_sel:WORD_1
	s_nop 1
	v_mfma_f32_16x16x4_f32 v[6:9], v2, v25, v[6:9]
	v_cvt_f32_f16_e32 v2, v10
	ds_read_b128 v[14:17], v123 offset:2560
	ds_read_b128 v[22:25], v123 offset:2816
	s_waitcnt lgkmcnt(1)
	v_mfma_f32_16x16x4_f32 v[6:9], v2, v14, v[6:9]
	v_cvt_f32_f16_sdwa v2, v10 dst_sel:DWORD dst_unused:UNUSED_PAD src0_sel:WORD_1
	s_nop 1
	v_mfma_f32_16x16x4_f32 v[6:9], v2, v15, v[6:9]
	v_cvt_f32_f16_e32 v2, v11
	s_nop 1
	v_mfma_f32_16x16x4_f32 v[6:9], v2, v16, v[6:9]
	v_cvt_f32_f16_sdwa v2, v11 dst_sel:DWORD dst_unused:UNUSED_PAD src0_sel:WORD_1
	s_nop 1
	v_mfma_f32_16x16x4_f32 v[6:9], v2, v17, v[6:9]
	v_cvt_f32_f16_e32 v2, v12
	s_waitcnt lgkmcnt(0)
	s_nop 0
	v_mfma_f32_16x16x4_f32 v[6:9], v2, v22, v[6:9]
	v_cvt_f32_f16_sdwa v2, v12 dst_sel:DWORD dst_unused:UNUSED_PAD src0_sel:WORD_1
	s_nop 1
	v_mfma_f32_16x16x4_f32 v[6:9], v2, v23, v[6:9]
	v_cvt_f32_f16_e32 v2, v13
	s_nop 0
	s_nop 0
	v_mfma_f32_16x16x4_f32 v[6:9], v2, v24, v[6:9]
	s_waitcnt vmcnt(9)
	v_mov_b64_e32 v[18:19], v[176:177]
	v_mov_b64_e32 v[20:21], v[178:179]
	v_cvt_f32_f16_e32 v2, v18
	v_mfma_f32_16x16x4_f32 v[6:9], v3, v25, v[6:9]
	ds_read_b128 v[14:17], v123 offset:3072
	ds_read_b128 v[22:25], v123 offset:3328
	s_waitcnt vmcnt(8)
	v_mov_b64_e32 v[10:11], v[180:181]
	v_mov_b64_e32 v[12:13], v[182:183]
	v_cvt_f32_f16_sdwa v3, v13 dst_sel:DWORD dst_unused:UNUSED_PAD src0_sel:WORD_1
	s_waitcnt lgkmcnt(1)
	v_mfma_f32_16x16x4_f32 v[6:9], v2, v14, v[6:9]
	v_cvt_f32_f16_sdwa v2, v18 dst_sel:DWORD dst_unused:UNUSED_PAD src0_sel:WORD_1
	s_nop 1
	v_mfma_f32_16x16x4_f32 v[6:9], v2, v15, v[6:9]
	v_cvt_f32_f16_e32 v2, v19
	s_nop 1
	v_mfma_f32_16x16x4_f32 v[6:9], v2, v16, v[6:9]
	v_cvt_f32_f16_sdwa v2, v19 dst_sel:DWORD dst_unused:UNUSED_PAD src0_sel:WORD_1
	s_nop 1
	v_mfma_f32_16x16x4_f32 v[6:9], v2, v17, v[6:9]
	v_cvt_f32_f16_e32 v2, v20
	s_nop 0
	s_waitcnt lgkmcnt(0)
	v_mfma_f32_16x16x4_f32 v[6:9], v2, v22, v[6:9]
	v_cvt_f32_f16_sdwa v2, v20 dst_sel:DWORD dst_unused:UNUSED_PAD src0_sel:WORD_1
	s_nop 1
	v_mfma_f32_16x16x4_f32 v[6:9], v2, v23, v[6:9]
	v_cvt_f32_f16_e32 v2, v21
	s_nop 1
	v_mfma_f32_16x16x4_f32 v[6:9], v2, v24, v[6:9]
	v_cvt_f32_f16_sdwa v2, v21 dst_sel:DWORD dst_unused:UNUSED_PAD src0_sel:WORD_1
	s_nop 1
	v_mfma_f32_16x16x4_f32 v[6:9], v2, v25, v[6:9]
	v_cvt_f32_f16_e32 v2, v10
	ds_read_b128 v[18:21], v123 offset:3584
	ds_read_b128 v[22:25], v123 offset:3840
	s_waitcnt lgkmcnt(1)
	v_mfma_f32_16x16x4_f32 v[6:9], v2, v18, v[6:9]
	v_cvt_f32_f16_sdwa v2, v10 dst_sel:DWORD dst_unused:UNUSED_PAD src0_sel:WORD_1
	s_nop 1
	v_mfma_f32_16x16x4_f32 v[6:9], v2, v19, v[6:9]
	v_cvt_f32_f16_e32 v2, v11
	s_nop 1
	v_mfma_f32_16x16x4_f32 v[6:9], v2, v20, v[6:9]
	v_cvt_f32_f16_sdwa v2, v11 dst_sel:DWORD dst_unused:UNUSED_PAD src0_sel:WORD_1
	s_nop 1
	v_mfma_f32_16x16x4_f32 v[6:9], v2, v21, v[6:9]
	v_cvt_f32_f16_e32 v2, v12
	s_waitcnt lgkmcnt(0)
	s_nop 0
	v_mfma_f32_16x16x4_f32 v[6:9], v2, v22, v[6:9]
	v_cvt_f32_f16_sdwa v2, v12 dst_sel:DWORD dst_unused:UNUSED_PAD src0_sel:WORD_1
	s_nop 1
	v_mfma_f32_16x16x4_f32 v[6:9], v2, v23, v[6:9]
	v_cvt_f32_f16_e32 v2, v13
	s_nop 0
	s_nop 0
	v_mfma_f32_16x16x4_f32 v[6:9], v2, v24, v[6:9]
	s_waitcnt vmcnt(7)
	v_mov_b64_e32 v[14:15], v[188:189]
	v_mov_b64_e32 v[16:17], v[190:191]
	v_cvt_f32_f16_e32 v2, v14
	v_mfma_f32_16x16x4_f32 v[6:9], v3, v25, v[6:9]
	ds_read_b128 v[18:21], v123 offset:4096
	ds_read_b128 v[22:25], v123 offset:4352
	s_waitcnt vmcnt(6)
	v_mov_b64_e32 v[10:11], v[192:193]
	v_mov_b64_e32 v[12:13], v[194:195]
	v_cvt_f32_f16_sdwa v3, v13 dst_sel:DWORD dst_unused:UNUSED_PAD src0_sel:WORD_1
	s_waitcnt lgkmcnt(1)
	v_mfma_f32_16x16x4_f32 v[6:9], v2, v18, v[6:9]
	v_cvt_f32_f16_sdwa v2, v14 dst_sel:DWORD dst_unused:UNUSED_PAD src0_sel:WORD_1
	s_nop 1
	v_mfma_f32_16x16x4_f32 v[6:9], v2, v19, v[6:9]
	v_cvt_f32_f16_e32 v2, v15
	s_nop 1
	v_mfma_f32_16x16x4_f32 v[6:9], v2, v20, v[6:9]
	v_cvt_f32_f16_sdwa v2, v15 dst_sel:DWORD dst_unused:UNUSED_PAD src0_sel:WORD_1
	s_nop 1
	v_mfma_f32_16x16x4_f32 v[6:9], v2, v21, v[6:9]
	v_cvt_f32_f16_e32 v2, v16
	s_nop 0
	s_waitcnt lgkmcnt(0)
	v_mfma_f32_16x16x4_f32 v[6:9], v2, v22, v[6:9]
	v_cvt_f32_f16_sdwa v2, v16 dst_sel:DWORD dst_unused:UNUSED_PAD src0_sel:WORD_1
	s_nop 1
	v_mfma_f32_16x16x4_f32 v[6:9], v2, v23, v[6:9]
	v_cvt_f32_f16_e32 v2, v17
	s_nop 1
	v_mfma_f32_16x16x4_f32 v[6:9], v2, v24, v[6:9]
	v_cvt_f32_f16_sdwa v2, v17 dst_sel:DWORD dst_unused:UNUSED_PAD src0_sel:WORD_1
	s_nop 1
	v_mfma_f32_16x16x4_f32 v[6:9], v2, v25, v[6:9]
	v_cvt_f32_f16_e32 v2, v10
	ds_read_b128 v[14:17], v123 offset:4608
	ds_read_b128 v[22:25], v123 offset:4864
	s_waitcnt lgkmcnt(1)
	v_mfma_f32_16x16x4_f32 v[6:9], v2, v14, v[6:9]
	v_cvt_f32_f16_sdwa v2, v10 dst_sel:DWORD dst_unused:UNUSED_PAD src0_sel:WORD_1
	s_nop 1
	v_mfma_f32_16x16x4_f32 v[6:9], v2, v15, v[6:9]
	v_cvt_f32_f16_e32 v2, v11
	s_nop 1
	v_mfma_f32_16x16x4_f32 v[6:9], v2, v16, v[6:9]
	v_cvt_f32_f16_sdwa v2, v11 dst_sel:DWORD dst_unused:UNUSED_PAD src0_sel:WORD_1
	s_nop 1
	v_mfma_f32_16x16x4_f32 v[6:9], v2, v17, v[6:9]
	v_cvt_f32_f16_e32 v2, v12
	s_waitcnt lgkmcnt(0)
	s_nop 0
	v_mfma_f32_16x16x4_f32 v[6:9], v2, v22, v[6:9]
	v_cvt_f32_f16_sdwa v2, v12 dst_sel:DWORD dst_unused:UNUSED_PAD src0_sel:WORD_1
	s_nop 1
	v_mfma_f32_16x16x4_f32 v[6:9], v2, v23, v[6:9]
	v_cvt_f32_f16_e32 v2, v13
	s_nop 0
	s_nop 0
	v_mfma_f32_16x16x4_f32 v[6:9], v2, v24, v[6:9]
	s_waitcnt vmcnt(5)
	v_mov_b64_e32 v[18:19], v[196:197]
	v_mov_b64_e32 v[20:21], v[198:199]
	v_cvt_f32_f16_e32 v2, v18
	v_mfma_f32_16x16x4_f32 v[6:9], v3, v25, v[6:9]
	ds_read_b128 v[14:17], v123 offset:5120
	ds_read_b128 v[22:25], v123 offset:5376
	s_waitcnt vmcnt(4)
	v_mov_b64_e32 v[10:11], v[200:201]
	v_mov_b64_e32 v[12:13], v[202:203]
	v_cvt_f32_f16_sdwa v3, v13 dst_sel:DWORD dst_unused:UNUSED_PAD src0_sel:WORD_1
	s_waitcnt lgkmcnt(1)
	v_mfma_f32_16x16x4_f32 v[6:9], v2, v14, v[6:9]
	v_cvt_f32_f16_sdwa v2, v18 dst_sel:DWORD dst_unused:UNUSED_PAD src0_sel:WORD_1
	s_nop 1
	v_mfma_f32_16x16x4_f32 v[6:9], v2, v15, v[6:9]
	v_cvt_f32_f16_e32 v2, v19
	s_nop 1
	v_mfma_f32_16x16x4_f32 v[6:9], v2, v16, v[6:9]
	v_cvt_f32_f16_sdwa v2, v19 dst_sel:DWORD dst_unused:UNUSED_PAD src0_sel:WORD_1
	s_nop 1
	v_mfma_f32_16x16x4_f32 v[6:9], v2, v17, v[6:9]
	v_cvt_f32_f16_e32 v2, v20
	s_nop 0
	s_waitcnt lgkmcnt(0)
	v_mfma_f32_16x16x4_f32 v[6:9], v2, v22, v[6:9]
	v_cvt_f32_f16_sdwa v2, v20 dst_sel:DWORD dst_unused:UNUSED_PAD src0_sel:WORD_1
	s_nop 1
	v_mfma_f32_16x16x4_f32 v[6:9], v2, v23, v[6:9]
	v_cvt_f32_f16_e32 v2, v21
	s_nop 1
	v_mfma_f32_16x16x4_f32 v[6:9], v2, v24, v[6:9]
	v_cvt_f32_f16_sdwa v2, v21 dst_sel:DWORD dst_unused:UNUSED_PAD src0_sel:WORD_1
	s_nop 1
	v_mfma_f32_16x16x4_f32 v[6:9], v2, v25, v[6:9]
	v_cvt_f32_f16_e32 v2, v10
	ds_read_b128 v[18:21], v123 offset:5632
	ds_read_b128 v[22:25], v123 offset:5888
	s_waitcnt lgkmcnt(1)
	v_mfma_f32_16x16x4_f32 v[6:9], v2, v18, v[6:9]
	v_cvt_f32_f16_sdwa v2, v10 dst_sel:DWORD dst_unused:UNUSED_PAD src0_sel:WORD_1
	s_nop 1
	v_mfma_f32_16x16x4_f32 v[6:9], v2, v19, v[6:9]
	v_cvt_f32_f16_e32 v2, v11
	s_nop 1
	v_mfma_f32_16x16x4_f32 v[6:9], v2, v20, v[6:9]
	v_cvt_f32_f16_sdwa v2, v11 dst_sel:DWORD dst_unused:UNUSED_PAD src0_sel:WORD_1
	s_nop 1
	v_mfma_f32_16x16x4_f32 v[6:9], v2, v21, v[6:9]
	v_cvt_f32_f16_e32 v2, v12
	s_waitcnt lgkmcnt(0)
	s_nop 0
	v_mfma_f32_16x16x4_f32 v[6:9], v2, v22, v[6:9]
	v_cvt_f32_f16_sdwa v2, v12 dst_sel:DWORD dst_unused:UNUSED_PAD src0_sel:WORD_1
	s_nop 1
	v_mfma_f32_16x16x4_f32 v[6:9], v2, v23, v[6:9]
	v_cvt_f32_f16_e32 v2, v13
	s_nop 0
	s_waitcnt vmcnt(2)
	v_mov_b64_e32 v[14:15], v[204:205]
	v_mov_b64_e32 v[16:17], v[206:207]
	v_mov_b64_e32 v[10:11], v[208:209]
	v_mov_b64_e32 v[12:13], v[210:211]
	v_cvt_f32_f16_sdwa v5, v13 dst_sel:DWORD dst_unused:UNUSED_PAD src0_sel:WORD_1
	v_mfma_f32_16x16x4_f32 v[6:9], v2, v24, v[6:9]
	v_cvt_f32_f16_e32 v2, v14
	v_mfma_f32_16x16x4_f32 v[6:9], v3, v25, v[6:9]
	ds_read_b128 v[18:21], v123 offset:6144
	ds_read_b128 v[22:25], v123 offset:6400
	s_waitcnt lgkmcnt(1)
	v_mfma_f32_16x16x4_f32 v[6:9], v2, v18, v[6:9]
	v_cvt_f32_f16_sdwa v2, v14 dst_sel:DWORD dst_unused:UNUSED_PAD src0_sel:WORD_1
	s_nop 1
	v_mfma_f32_16x16x4_f32 v[6:9], v2, v19, v[6:9]
	v_cvt_f32_f16_e32 v2, v15
	s_nop 1
	v_mfma_f32_16x16x4_f32 v[6:9], v2, v20, v[6:9]
	v_cvt_f32_f16_sdwa v2, v15 dst_sel:DWORD dst_unused:UNUSED_PAD src0_sel:WORD_1
	s_nop 1
	v_mfma_f32_16x16x4_f32 v[6:9], v2, v21, v[6:9]
	v_cvt_f32_f16_e32 v2, v16
	s_nop 0
	s_waitcnt lgkmcnt(0)
	v_mfma_f32_16x16x4_f32 v[6:9], v2, v22, v[6:9]
	v_cvt_f32_f16_sdwa v2, v16 dst_sel:DWORD dst_unused:UNUSED_PAD src0_sel:WORD_1
	s_nop 1
	v_mfma_f32_16x16x4_f32 v[6:9], v2, v23, v[6:9]
	v_cvt_f32_f16_e32 v2, v17
	s_nop 1
	v_mfma_f32_16x16x4_f32 v[6:9], v2, v24, v[6:9]
	v_cvt_f32_f16_sdwa v2, v17 dst_sel:DWORD dst_unused:UNUSED_PAD src0_sel:WORD_1
	s_nop 1
	v_mfma_f32_16x16x4_f32 v[6:9], v2, v25, v[6:9]
	v_cvt_f32_f16_e32 v2, v10
	ds_read_b128 v[14:17], v123 offset:6656
	ds_read_b128 v[22:25], v123 offset:6912
	s_waitcnt lgkmcnt(1)
	v_mfma_f32_16x16x4_f32 v[6:9], v2, v14, v[6:9]
	v_cvt_f32_f16_sdwa v2, v10 dst_sel:DWORD dst_unused:UNUSED_PAD src0_sel:WORD_1
	s_nop 1
	v_mfma_f32_16x16x4_f32 v[6:9], v2, v15, v[6:9]
	v_cvt_f32_f16_e32 v2, v11
	s_nop 1
	v_mfma_f32_16x16x4_f32 v[6:9], v2, v16, v[6:9]
	v_cvt_f32_f16_sdwa v2, v11 dst_sel:DWORD dst_unused:UNUSED_PAD src0_sel:WORD_1
	s_nop 1
	v_mfma_f32_16x16x4_f32 v[6:9], v2, v17, v[6:9]
	v_cvt_f32_f16_e32 v2, v12
	s_waitcnt lgkmcnt(0)
	s_nop 0
	v_mfma_f32_16x16x4_f32 v[6:9], v2, v22, v[6:9]
	v_cvt_f32_f16_sdwa v2, v12 dst_sel:DWORD dst_unused:UNUSED_PAD src0_sel:WORD_1
	s_nop 1
	v_mfma_f32_16x16x4_f32 v[6:9], v2, v23, v[6:9]
	v_cvt_f32_f16_e32 v2, v13
	s_nop 1
	v_mfma_f32_16x16x4_f32 v[6:9], v2, v24, v[6:9]
	s_nop 0
	ds_read_b128 v[10:13], v123 offset:7168
	ds_read_b128 v[14:17], v123 offset:7424
	v_mfma_f32_16x16x4_f32 v[6:9], v5, v25, v[6:9]
	s_waitcnt vmcnt(1)
	v_mov_b64_e32 v[18:19], v[212:213]
	v_mov_b64_e32 v[20:21], v[214:215]
	v_cvt_f32_f16_e32 v5, v18
	s_waitcnt lgkmcnt(1)
	s_nop 0
	v_mfma_f32_16x16x4_f32 v[6:9], v5, v10, v[6:9]
	v_cvt_f32_f16_sdwa v5, v18 dst_sel:DWORD dst_unused:UNUSED_PAD src0_sel:WORD_1
	s_nop 1
	v_mfma_f32_16x16x4_f32 v[6:9], v5, v11, v[6:9]
	v_cvt_f32_f16_e32 v5, v19
	s_nop 1
	v_mfma_f32_16x16x4_f32 v[6:9], v5, v12, v[6:9]
	v_cvt_f32_f16_sdwa v5, v19 dst_sel:DWORD dst_unused:UNUSED_PAD src0_sel:WORD_1
	s_nop 1
	v_mfma_f32_16x16x4_f32 v[6:9], v5, v13, v[6:9]
	v_cvt_f32_f16_e32 v5, v20
	s_waitcnt lgkmcnt(0)
	s_nop 0
	v_mfma_f32_16x16x4_f32 v[6:9], v5, v14, v[6:9]
	v_cvt_f32_f16_sdwa v5, v20 dst_sel:DWORD dst_unused:UNUSED_PAD src0_sel:WORD_1
	s_nop 1
	v_mfma_f32_16x16x4_f32 v[6:9], v5, v15, v[6:9]
	v_cvt_f32_f16_e32 v5, v21
	s_nop 1
	v_mfma_f32_16x16x4_f32 v[6:9], v5, v16, v[6:9]
	v_cvt_f32_f16_sdwa v5, v21 dst_sel:DWORD dst_unused:UNUSED_PAD src0_sel:WORD_1
	s_nop 1
	v_mfma_f32_16x16x4_f32 v[6:9], v5, v17, v[6:9]
	s_waitcnt vmcnt(0)
	v_mov_b64_e32 v[0:1], v[216:217]
	v_mov_b64_e32 v[2:3], v[218:219]
	v_cvt_f32_f16_e32 v5, v0
	ds_read_b128 v[10:13], v123 offset:7680
	ds_read_b128 v[14:17], v123 offset:7936
	v_cvt_f32_f16_sdwa v0, v0 dst_sel:DWORD dst_unused:UNUSED_PAD src0_sel:WORD_1
	s_waitcnt lgkmcnt(0)
	s_barrier
	v_mfma_f32_16x16x4_f32 v[6:9], v5, v10, v[6:9]
	v_mfma_f32_16x16x4_f32 v[6:9], v0, v11, v[6:9]
	v_cvt_f32_f16_e32 v0, v1
	s_nop 1
	v_mfma_f32_16x16x4_f32 v[6:9], v0, v12, v[6:9]
	v_cvt_f32_f16_sdwa v0, v1 dst_sel:DWORD dst_unused:UNUSED_PAD src0_sel:WORD_1
	s_nop 1
	v_mfma_f32_16x16x4_f32 v[6:9], v0, v13, v[6:9]
	v_cvt_f32_f16_e32 v0, v2
	s_nop 1
	v_mfma_f32_16x16x4_f32 v[6:9], v0, v14, v[6:9]
	v_cvt_f32_f16_sdwa v0, v2 dst_sel:DWORD dst_unused:UNUSED_PAD src0_sel:WORD_1
	s_nop 1
	v_mfma_f32_16x16x4_f32 v[6:9], v0, v15, v[6:9]
	v_cvt_f32_f16_e32 v0, v3
	s_nop 1
	v_mfma_f32_16x16x4_f32 v[6:9], v0, v16, v[6:9]
	v_cvt_f32_f16_sdwa v0, v3 dst_sel:DWORD dst_unused:UNUSED_PAD src0_sel:WORD_1
	s_nop 1
	v_mfma_f32_16x16x4_f32 v[0:3], v0, v17, v[6:9]
	s_and_saveexec_b64 s[0:1], s[14:15]
	s_nop 8
	ds_write_b128 v126, v[0:3]
	s_or_b64 exec, exec, s[0:1]
	s_waitcnt lgkmcnt(0)
	s_barrier
	s_and_saveexec_b64 s[0:1], s[12:13]
	s_cbranch_execz .LBB0_628
	ds_read_b128 v[6:9], v126
	ds_read_b32 v5, v113
	ds_read_b128 v[10:13], v124
	v_and_or_b32 v4, v4, s55, v114
	v_lshlrev_b32_e32 v34, 2, v4
	s_waitcnt lgkmcnt(2)
	v_add_f32_e32 v0, v0, v6
	v_add_f32_e32 v1, v1, v7
	s_waitcnt lgkmcnt(0)
	v_fma_f32 v0, v0, v10, v5
	ds_bpermute_b32 v6, v109, v0
	v_fma_f32 v1, v1, v11, v5
	v_add_f32_e32 v2, v2, v8
	v_fma_f32 v2, v2, v12, v5
	v_add_f32_e32 v3, v3, v9
	ds_bpermute_b32 v7, v109, v1
	v_fmac_f32_e32 v5, v3, v13
	s_waitcnt lgkmcnt(1)
	v_max_f32_e32 v3, v6, v6
	ds_bpermute_b32 v6, v109, v2
	v_max_f32_e32 v3, v0, v3
	s_waitcnt lgkmcnt(1)
	v_max_f32_e32 v7, v7, v7
	ds_bpermute_b32 v8, v109, v5
	v_max_f32_e32 v7, v1, v7
	s_waitcnt lgkmcnt(1)
	v_max_f32_e32 v6, v6, v6
	ds_bpermute_b32 v9, v108, v3
	v_max_f32_e32 v6, v2, v6
	ds_bpermute_b32 v10, v108, v7
	ds_bpermute_b32 v11, v108, v6
	s_waitcnt lgkmcnt(3)
	v_max_f32_e32 v8, v8, v8
	v_max_f32_e32 v8, v5, v8
	s_waitcnt lgkmcnt(2)
	v_max_f32_e32 v9, v9, v9
	v_max_f32_e32 v3, v3, v9
	s_waitcnt lgkmcnt(1)
	v_max_f32_e32 v9, v10, v10
	ds_bpermute_b32 v10, v108, v8
	v_max_f32_e32 v7, v7, v9
	s_waitcnt lgkmcnt(1)
	v_max_f32_e32 v9, v11, v11
	ds_bpermute_b32 v11, v107, v3
	v_max_f32_e32 v6, v6, v9
	s_waitcnt lgkmcnt(1)
	v_max_f32_e32 v9, v10, v10
	ds_bpermute_b32 v10, v107, v7
	v_max_f32_e32 v8, v8, v9
	s_waitcnt lgkmcnt(1)
	v_max_f32_e32 v9, v11, v11
	ds_bpermute_b32 v11, v107, v6
	v_max_f32_e32 v3, v3, v9
	s_waitcnt lgkmcnt(1)
	v_max_f32_e32 v9, v10, v10
	v_max_f32_e32 v7, v7, v9
	ds_bpermute_b32 v10, v107, v8
	s_waitcnt lgkmcnt(1)
	v_max_f32_e32 v9, v11, v11
	v_max_f32_e32 v6, v6, v9
	ds_bpermute_b32 v9, v106, v3
	ds_bpermute_b32 v11, v106, v7
	s_waitcnt lgkmcnt(2)
	v_max_f32_e32 v10, v10, v10
	v_max_f32_e32 v8, v8, v10
	ds_bpermute_b32 v10, v106, v6
	s_waitcnt lgkmcnt(2)
	v_max_f32_e32 v9, v9, v9
	v_max_f32_e32 v3, v3, v9
	v_sub_f32_e32 v0, v0, v3
	v_mul_f32_e32 v3, 0x3fb8aa3b, v0
	s_waitcnt lgkmcnt(1)
	v_max_f32_e32 v9, v11, v11
	v_fma_f32 v11, v0, s51, -v3
	v_rndne_f32_e32 v12, v3
	v_fmac_f32_e32 v11, 0x32a5705f, v0
	v_sub_f32_e32 v3, v3, v12
	v_add_f32_e32 v3, v3, v11
	v_exp_f32_e32 v3, v3
	v_cvt_i32_f32_e32 v11, v12
	v_max_f32_e32 v7, v7, v9
	s_waitcnt lgkmcnt(0)
	v_max_f32_e32 v9, v10, v10
	ds_bpermute_b32 v10, v106, v8
	v_ldexp_f32 v3, v3, v11
	v_cmp_ngt_f32_e32 vcc, s53, v0
	v_sub_f32_e32 v1, v1, v7
	v_max_f32_e32 v6, v6, v9
	v_cndmask_b32_e32 v3, 0, v3, vcc
	v_cmp_nlt_f32_e32 vcc, s54, v0
	s_waitcnt lgkmcnt(0)
	v_max_f32_e32 v9, v10, v10
	v_max_f32_e32 v8, v8, v9
	v_cndmask_b32_e32 v0, v127, v3, vcc
	v_mul_f32_e32 v3, 0x3fb8aa3b, v1
	v_fma_f32 v7, v1, s51, -v3
	v_rndne_f32_e32 v9, v3
	v_sub_f32_e32 v2, v2, v6
	v_fmac_f32_e32 v7, 0x32a5705f, v1
	v_sub_f32_e32 v3, v3, v9
	v_mul_f32_e32 v6, 0x3fb8aa3b, v2
	v_add_f32_e32 v3, v3, v7
	v_cvt_i32_f32_e32 v7, v9
	v_fma_f32 v9, v2, s51, -v6
	v_rndne_f32_e32 v10, v6
	v_fmac_f32_e32 v9, 0x32a5705f, v2
	v_sub_f32_e32 v6, v6, v10
	v_exp_f32_e32 v3, v3
	v_add_f32_e32 v6, v6, v9
	v_exp_f32_e32 v6, v6
	v_cvt_i32_f32_e32 v9, v10
	v_ldexp_f32 v3, v3, v7
	v_cmp_ngt_f32_e32 vcc, s53, v1
	v_sub_f32_e32 v5, v5, v8
	s_nop 0
	v_cndmask_b32_e32 v10, 0, v3, vcc
	v_ldexp_f32 v3, v6, v9
	v_mul_f32_e32 v6, 0x3fb8aa3b, v5
	v_fma_f32 v7, v5, s51, -v6
	v_rndne_f32_e32 v8, v6
	v_fmac_f32_e32 v7, 0x32a5705f, v5
	v_sub_f32_e32 v6, v6, v8
	v_add_f32_e32 v6, v6, v7
	v_exp_f32_e32 v6, v6
	v_cvt_i32_f32_e32 v7, v8
	v_cmp_ngt_f32_e32 vcc, s53, v2
	ds_bpermute_b32 v8, v109, v0
	s_nop 0
	v_cndmask_b32_e32 v3, 0, v3, vcc
	v_cmp_nlt_f32_e32 vcc, s54, v2
	s_nop 1
	v_cndmask_b32_e32 v2, v127, v3, vcc
	v_ldexp_f32 v3, v6, v7
	v_cmp_ngt_f32_e32 vcc, s53, v5
	ds_bpermute_b32 v6, v109, v2
	s_nop 0
	v_cndmask_b32_e32 v3, 0, v3, vcc
	v_cmp_nlt_f32_e32 vcc, s54, v5
	s_nop 1
	v_cndmask_b32_e32 v3, v127, v3, vcc
	ds_bpermute_b32 v7, v109, v3
	v_cmp_nlt_f32_e32 vcc, s54, v1
	s_waitcnt lgkmcnt(0)
	v_pk_add_f32 v[6:7], v[2:3], v[6:7]
	v_cndmask_b32_e32 v1, v127, v10, vcc
	ds_bpermute_b32 v10, v108, v6
	ds_bpermute_b32 v11, v108, v7
	ds_bpermute_b32 v9, v109, v1
	s_waitcnt lgkmcnt(1)
	v_pk_add_f32 v[6:7], v[6:7], v[10:11]
	ds_bpermute_b32 v10, v107, v6
	ds_bpermute_b32 v11, v107, v7
	s_waitcnt lgkmcnt(2)
	v_pk_add_f32 v[8:9], v[0:1], v[8:9]
	ds_bpermute_b32 v12, v108, v8
	ds_bpermute_b32 v13, v108, v9
	s_waitcnt lgkmcnt(2)
	v_pk_add_f32 v[6:7], v[6:7], v[10:11]
	ds_bpermute_b32 v10, v106, v6
	ds_bpermute_b32 v11, v106, v7
	s_waitcnt lgkmcnt(2)
	v_pk_add_f32 v[8:9], v[8:9], v[12:13]
	ds_bpermute_b32 v12, v107, v8
	ds_bpermute_b32 v13, v107, v9
	s_waitcnt lgkmcnt(2)
	v_pk_add_f32 v[6:7], v[6:7], v[10:11]
	s_nop 0
	v_div_scale_f32 v5, s[34:35], v7, v7, v3
	s_waitcnt lgkmcnt(0)
	v_pk_add_f32 v[8:9], v[8:9], v[12:13]
	v_rcp_f32_e32 v10, v5
	ds_bpermute_b32 v12, v106, v8
	ds_bpermute_b32 v13, v106, v9
	v_fma_f32 v11, -v5, v10, 1.0
	v_fmac_f32_e32 v10, v11, v10
	v_div_scale_f32 v11, vcc, v3, v7, v3
	s_waitcnt lgkmcnt(0)
	v_pk_add_f32 v[8:9], v[8:9], v[12:13]
	v_mul_f32_e32 v12, v11, v10
	v_fma_f32 v13, -v5, v12, v11
	v_fmac_f32_e32 v12, v13, v10
	v_fma_f32 v5, -v5, v12, v11
	v_div_scale_f32 v11, s[34:35], v6, v6, v2
	v_rcp_f32_e32 v13, v11
	v_div_fmas_f32 v5, v5, v10, v12
	v_div_fixup_f32 v3, v5, v7, v3
	v_fma_f32 v5, -v11, v13, 1.0
	v_fmac_f32_e32 v13, v5, v13
	v_div_scale_f32 v5, vcc, v2, v6, v2
	v_mul_f32_e32 v7, v5, v13
	v_fma_f32 v10, -v11, v7, v5
	v_fmac_f32_e32 v7, v10, v13
	v_div_scale_f32 v10, s[34:35], v9, v9, v1
	v_fma_f32 v5, -v11, v7, v5
	v_rcp_f32_e32 v11, v10
	v_div_fmas_f32 v5, v5, v13, v7
	v_div_fixup_f32 v2, v5, v6, v2
	v_fma_f32 v5, -v10, v11, 1.0
	v_fmac_f32_e32 v11, v5, v11
	v_div_scale_f32 v5, vcc, v1, v9, v1
	v_mul_f32_e32 v6, v5, v11
	v_fma_f32 v7, -v10, v6, v5
	v_fmac_f32_e32 v6, v7, v11
	v_div_scale_f32 v7, s[34:35], v8, v8, v0
	v_fma_f32 v5, -v10, v6, v5
	v_rcp_f32_e32 v10, v7
	v_div_fmas_f32 v5, v5, v11, v6
	v_div_fixup_f32 v1, v5, v9, v1
	v_fma_f32 v5, -v7, v10, 1.0
	v_fmac_f32_e32 v10, v5, v10
	v_div_scale_f32 v5, vcc, v0, v8, v0
	v_mul_f32_e32 v6, v5, v10
	v_fma_f32 v9, -v7, v6, v5
	v_fmac_f32_e32 v6, v9, v10
	v_fma_f32 v5, -v7, v6, v5
	v_div_fmas_f32 v5, v5, v10, v6
	v_lshl_or_b32 v6, s57, 4, v111
	v_ashrrev_i32_e32 v7, 31, v6
	v_lshlrev_b64 v[6:7], 15, v[6:7]
	v_lshl_add_u64 v[6:7], s[28:29], 0, v[6:7]
	v_div_fixup_f32 v0, v5, v8, v0
	v_lshl_add_u64 v[4:5], v[6:7], 0, v[34:35]
	global_store_dwordx4 v[4:5], v[0:3], off
	s_branch .LBB0_628
